# weight-conversion loop in the mixer phase: each register set waits only for its own loads (true two-deep pipeline)
# speedup vs baseline: 1.0020x; 1.0020x over previous
.LBB0_996:
	s_and_b32 s26, s11, 0x380
	v_add_u32_e32 v0, s26, v135
	v_mad_i64_i32 v[66:67], s[62:63], s34, v0, 0
	v_lshl_add_u64 v[66:67], v[66:67], 2, s[8:9]
	s_mov_b32 s25, s71
	v_lshl_add_u64 v[66:67], s[24:25], 2, v[66:67]
	v_lshlrev_b32_e32 v0, 2, v134
	v_lshl_add_u64 v[66:67], v[66:67], 0, v[0:1]
	s_lshl_b32 s8, s34, 2
	s_mov_b32 s9, s71
	v_lshl_add_u64 v[74:75], v[66:67], 0, s[8:9]
	global_load_dwordx4 v[70:73], v[66:67], off nt
	s_nop 0
	global_load_dwordx4 v[66:69], v[74:75], off nt
	v_lshl_add_u64 v[74:75], v[74:75], 0, s[8:9]
	v_lshl_add_u64 v[82:83], v[74:75], 0, s[8:9]
	global_load_dwordx4 v[78:81], v[74:75], off nt
	s_nop 0
	global_load_dwordx4 v[74:77], v[82:83], off nt
	v_lshl_add_u64 v[82:83], v[82:83], 0, s[8:9]
	v_lshl_add_u64 v[90:91], v[82:83], 0, s[8:9]
	global_load_dwordx4 v[86:89], v[82:83], off nt
	s_nop 0
	global_load_dwordx4 v[82:85], v[90:91], off nt
	v_lshl_add_u64 v[90:91], v[90:91], 0, s[8:9]
	v_lshl_add_u64 v[98:99], v[90:91], 0, s[8:9]
	v_lshl_add_u64 v[102:103], v[98:99], 0, s[8:9]
	v_lshl_add_u64 v[106:107], v[102:103], 0, s[8:9]
	v_lshl_add_u64 v[110:111], v[106:107], 0, s[8:9]
	v_lshl_add_u64 v[114:115], v[110:111], 0, s[8:9]
	v_lshl_add_u64 v[118:119], v[114:115], 0, s[8:9]
	v_lshl_add_u64 v[122:123], v[118:119], 0, s[8:9]
	v_lshl_add_u64 v[126:127], v[122:123], 0, s[8:9]
	global_load_dwordx4 v[94:97], v[90:91], off nt
	s_nop 0
	global_load_dwordx4 v[90:93], v[98:99], off nt
	s_nop 0
	global_load_dwordx4 v[98:101], v[102:103], off nt
	s_nop 0
	global_load_dwordx4 v[102:105], v[106:107], off nt
	s_nop 0
	global_load_dwordx4 v[106:109], v[110:111], off nt
	s_nop 0
	global_load_dwordx4 v[110:113], v[114:115], off nt
	s_nop 0
	global_load_dwordx4 v[114:117], v[118:119], off nt
	s_nop 0
	global_load_dwordx4 v[118:121], v[122:123], off nt
	s_nop 0
	global_load_dwordx4 v[122:125], v[126:127], off nt
	v_lshl_add_u64 v[126:127], v[126:127], 0, s[8:9]
	global_load_dwordx4 v[126:129], v[126:127], off nt
	s_waitcnt vmcnt(16)
	s_branch .Lcvm_a_ready

.Lcvm_a_ready:
	v_mul_f32_e32 v0, 0x42800000, v2
	v_mul_f32_e32 v131, 0x42800000, v6
	v_mov_b32_e32 v130, v1
	v_cvt_pk_fp8_f32 v130, v0, v131
	v_mul_f32_e32 v132, 0x42800000, v10
	v_mul_f32_e32 v133, 0x42800000, v14
	v_mul_f32_e32 v0, 0x42800000, v18
	v_cvt_pk_fp8_f32 v130, v132, v133 op_sel:[0,0,1]
	v_mul_f32_e32 v132, 0x42800000, v22
	v_mov_b32_e32 v131, v1
	v_cvt_pk_fp8_f32 v131, v0, v132
	v_mul_f32_e32 v133, 0x42800000, v26
	v_mul_f32_e32 v138, 0x42800000, v30
	v_mul_f32_e32 v0, 0x42800000, v34
	v_cvt_pk_fp8_f32 v131, v133, v138 op_sel:[0,0,1]
	v_mul_f32_e32 v133, 0x42800000, v38
	v_mov_b32_e32 v132, v1
	v_cvt_pk_fp8_f32 v132, v0, v133
	v_mul_f32_e32 v138, 0x42800000, v42
	v_mul_f32_e32 v139, 0x42800000, v46
	v_mul_f32_e32 v0, 0x42800000, v50
	v_cvt_pk_fp8_f32 v132, v138, v139 op_sel:[0,0,1]
	v_mul_f32_e32 v138, 0x42800000, v54
	v_mov_b32_e32 v133, v1
	v_cvt_pk_fp8_f32 v133, v0, v138
	v_mul_f32_e32 v139, 0x42800000, v58
	v_mul_f32_e32 v149, 0x42800000, v62
	v_mul_f32_e32 v0, 0x42800000, v3
	v_cvt_pk_fp8_f32 v133, v139, v149 op_sel:[0,0,1]
	v_mul_f32_e32 v138, 0x42800000, v31
	v_mul_f32_e32 v139, 0x42800000, v47
	v_mul_f32_e32 v149, 0x42800000, v63
	ds_write_b128 v144, v[130:133]
	v_mul_f32_e32 v131, 0x42800000, v7
	v_mov_b32_e32 v130, v1
	v_cvt_pk_fp8_f32 v130, v0, v131
	v_mul_f32_e32 v132, 0x42800000, v11
	v_mul_f32_e32 v133, 0x42800000, v15
	v_mul_f32_e32 v0, 0x42800000, v19
	v_cvt_pk_fp8_f32 v130, v132, v133 op_sel:[0,0,1]
	v_mul_f32_e32 v132, 0x42800000, v23
	v_mov_b32_e32 v131, v1
	v_cvt_pk_fp8_f32 v131, v0, v132
	v_mul_f32_e32 v133, 0x42800000, v27
	v_mul_f32_e32 v0, 0x42800000, v35
	v_mov_b32_e32 v132, v1
	v_cvt_pk_fp8_f32 v131, v133, v138 op_sel:[0,0,1]
	v_mul_f32_e32 v133, 0x42800000, v39
	v_cvt_pk_fp8_f32 v132, v0, v133
	v_mul_f32_e32 v138, 0x42800000, v43
	v_mul_f32_e32 v0, 0x42800000, v51
	v_mov_b32_e32 v133, v1
	v_cvt_pk_fp8_f32 v132, v138, v139 op_sel:[0,0,1]
	v_mul_f32_e32 v138, 0x42800000, v55
	v_cvt_pk_fp8_f32 v133, v0, v138
	v_mul_f32_e32 v139, 0x42800000, v59
	v_mul_f32_e32 v0, 0x42800000, v4
	v_mul_f32_e32 v138, 0x42800000, v32
	v_cvt_pk_fp8_f32 v133, v139, v149 op_sel:[0,0,1]
	v_mul_f32_e32 v139, 0x42800000, v48
	v_mul_f32_e32 v149, 0x42800000, v64
	s_cmp_lg_u32 s36, 0
	ds_write_b128 v144, v[130:133] offset:128
	v_mul_f32_e32 v131, 0x42800000, v8
	v_mov_b32_e32 v130, v1
	v_cvt_pk_fp8_f32 v130, v0, v131
	v_mul_f32_e32 v132, 0x42800000, v12
	v_mul_f32_e32 v133, 0x42800000, v16
	v_mul_f32_e32 v0, 0x42800000, v20
	v_cvt_pk_fp8_f32 v130, v132, v133 op_sel:[0,0,1]
	v_mul_f32_e32 v132, 0x42800000, v24
	v_mov_b32_e32 v131, v1
	v_cvt_pk_fp8_f32 v131, v0, v132
	v_mul_f32_e32 v133, 0x42800000, v28
	v_mul_f32_e32 v0, 0x42800000, v36
	v_mov_b32_e32 v132, v1
	v_cvt_pk_fp8_f32 v131, v133, v138 op_sel:[0,0,1]
	v_mul_f32_e32 v133, 0x42800000, v40
	v_cvt_pk_fp8_f32 v132, v0, v133
	v_mul_f32_e32 v138, 0x42800000, v44
	v_mul_f32_e32 v0, 0x42800000, v52
	v_mov_b32_e32 v133, v1
	v_cvt_pk_fp8_f32 v132, v138, v139 op_sel:[0,0,1]
	v_mul_f32_e32 v138, 0x42800000, v56
	v_cvt_pk_fp8_f32 v133, v0, v138
	v_mul_f32_e32 v139, 0x42800000, v60
	v_mul_f32_e32 v0, 0x42800000, v5
	v_mul_f32_e32 v138, 0x42800000, v33
	v_cvt_pk_fp8_f32 v133, v139, v149 op_sel:[0,0,1]
	v_mul_f32_e32 v139, 0x42800000, v49
	v_mul_f32_e32 v149, 0x42800000, v65
	s_cselect_b64 s[34:35], -1, 0
	ds_write_b128 v144, v[130:133] offset:256
	v_mul_f32_e32 v131, 0x42800000, v9
	v_mov_b32_e32 v130, v1
	v_cvt_pk_fp8_f32 v130, v0, v131
	v_mul_f32_e32 v132, 0x42800000, v13
	v_mul_f32_e32 v133, 0x42800000, v17
	v_mul_f32_e32 v0, 0x42800000, v21
	v_cvt_pk_fp8_f32 v130, v132, v133 op_sel:[0,0,1]
	v_mul_f32_e32 v132, 0x42800000, v25
	v_mov_b32_e32 v131, v1
	v_cvt_pk_fp8_f32 v131, v0, v132
	v_mul_f32_e32 v133, 0x42800000, v29
	v_mul_f32_e32 v0, 0x42800000, v37
	v_mov_b32_e32 v132, v1
	v_cvt_pk_fp8_f32 v131, v133, v138 op_sel:[0,0,1]
	v_mul_f32_e32 v133, 0x42800000, v41
	v_cvt_pk_fp8_f32 v132, v0, v133
	v_mul_f32_e32 v138, 0x42800000, v45
	v_mul_f32_e32 v0, 0x42800000, v53
	v_mov_b32_e32 v133, v1
	v_cvt_pk_fp8_f32 v132, v138, v139 op_sel:[0,0,1]
	v_mul_f32_e32 v138, 0x42800000, v57
	v_cvt_pk_fp8_f32 v133, v0, v138
	v_mul_f32_e32 v139, 0x42800000, v61
	v_add_u32_e32 v138, s10, v140
	s_cmp_eq_u32 s36, 0
	v_cvt_pk_fp8_f32 v133, v139, v149 op_sel:[0,0,1]
	ds_write_b128 v144, v[130:133] offset:384
	s_waitcnt lgkmcnt(0)
	s_barrier
	ds_read_b128 v[130:133], v145
	s_cbranch_scc1 .LBB0_1003
	v_cmp_lt_i32_e32 vcc, s47, v138
	v_lshlrev_b32_e32 v0, 1, v138
	v_and_b32_e32 v139, 0x7f, v138
	s_and_saveexec_b64 s[8:9], vcc
	s_xor_b64 s[8:9], exec, s[8:9]
	v_add_u32_e32 v0, 0x7ffff800, v0
	v_and_b32_e32 v0, 0x7fffff00, v0
	v_or3_b32 v138, v139, v0, s64
	s_andn2_saveexec_b64 s[8:9], s[8:9]
	v_and_or_b32 v138, v0, s65, v139
	s_or_b64 exec, exec, s[8:9]

.LBB0_1028:
	s_and_b32 s25, s11, 0x380
	v_add_u32_e32 v0, s25, v135
	v_mad_i64_i32 v[2:3], s[62:63], s34, v0, 0
	v_lshl_add_u64 v[2:3], v[2:3], 2, s[8:9]
	s_mov_b32 s11, s71
	v_lshl_add_u64 v[2:3], s[10:11], 2, v[2:3]
	v_lshlrev_b32_e32 v0, 2, v134
	v_lshl_add_u64 v[2:3], v[2:3], 0, v[0:1]
	s_lshl_b32 s70, s34, 2
	v_lshl_add_u64 v[10:11], v[2:3], 0, s[70:71]
	global_load_dwordx4 v[2:5], v[2:3], off nt
	s_nop 0
	global_load_dwordx4 v[6:9], v[10:11], off nt
	v_lshl_add_u64 v[10:11], v[10:11], 0, s[70:71]
	v_lshl_add_u64 v[18:19], v[10:11], 0, s[70:71]
	global_load_dwordx4 v[10:13], v[10:11], off nt
	s_nop 0
	global_load_dwordx4 v[14:17], v[18:19], off nt
	v_lshl_add_u64 v[18:19], v[18:19], 0, s[70:71]
	v_lshl_add_u64 v[26:27], v[18:19], 0, s[70:71]
	global_load_dwordx4 v[18:21], v[18:19], off nt
	s_nop 0
	global_load_dwordx4 v[22:25], v[26:27], off nt
	v_lshl_add_u64 v[26:27], v[26:27], 0, s[70:71]
	v_lshl_add_u64 v[34:35], v[26:27], 0, s[70:71]
	v_lshl_add_u64 v[38:39], v[34:35], 0, s[70:71]
	v_lshl_add_u64 v[42:43], v[38:39], 0, s[70:71]
	v_lshl_add_u64 v[46:47], v[42:43], 0, s[70:71]
	v_lshl_add_u64 v[50:51], v[46:47], 0, s[70:71]
	v_lshl_add_u64 v[54:55], v[50:51], 0, s[70:71]
	v_lshl_add_u64 v[58:59], v[54:55], 0, s[70:71]
	v_lshl_add_u64 v[62:63], v[58:59], 0, s[70:71]
	global_load_dwordx4 v[26:29], v[26:27], off nt
	s_nop 0
	global_load_dwordx4 v[30:33], v[34:35], off nt
	s_nop 0
	global_load_dwordx4 v[34:37], v[38:39], off nt
	s_nop 0
	global_load_dwordx4 v[38:41], v[42:43], off nt
	s_nop 0
	global_load_dwordx4 v[42:45], v[46:47], off nt
	s_nop 0
	global_load_dwordx4 v[46:49], v[50:51], off nt
	s_nop 0
	global_load_dwordx4 v[50:53], v[54:55], off nt
	s_nop 0
	global_load_dwordx4 v[54:57], v[58:59], off nt
	s_nop 0
	global_load_dwordx4 v[58:61], v[62:63], off nt
	v_lshl_add_u64 v[62:63], v[62:63], 0, s[70:71]
	global_load_dwordx4 v[62:65], v[62:63], off nt
	s_mov_b32 s70, s25
	s_waitcnt vmcnt(16)
	s_branch .Lcvm_b_ready
.LBB0_1029:
	s_waitcnt vmcnt(0)
.Lcvm_b_ready:
	v_mul_f32_e32 v0, 0x42800000, v70
	v_mul_f32_e32 v131, 0x42800000, v66
	v_mov_b32_e32 v130, v1
	v_cvt_pk_fp8_f32 v130, v0, v131
	v_mul_f32_e32 v132, 0x42800000, v78
	v_mul_f32_e32 v133, 0x42800000, v74
	v_mul_f32_e32 v0, 0x42800000, v86
	v_cvt_pk_fp8_f32 v130, v132, v133 op_sel:[0,0,1]
	v_mul_f32_e32 v132, 0x42800000, v82
	v_mov_b32_e32 v131, v1
	v_cvt_pk_fp8_f32 v131, v0, v132
	v_mul_f32_e32 v133, 0x42800000, v94
	v_mul_f32_e32 v138, 0x42800000, v90
	v_mul_f32_e32 v0, 0x42800000, v98
	v_cvt_pk_fp8_f32 v131, v133, v138 op_sel:[0,0,1]
	v_mul_f32_e32 v133, 0x42800000, v102
	v_mov_b32_e32 v132, v1
	v_cvt_pk_fp8_f32 v132, v0, v133
	v_mul_f32_e32 v138, 0x42800000, v106
	v_mul_f32_e32 v139, 0x42800000, v110
	v_mul_f32_e32 v0, 0x42800000, v114
	v_cvt_pk_fp8_f32 v132, v138, v139 op_sel:[0,0,1]
	v_mul_f32_e32 v138, 0x42800000, v118
	v_mov_b32_e32 v133, v1
	v_cvt_pk_fp8_f32 v133, v0, v138
	v_mul_f32_e32 v139, 0x42800000, v122
	v_mul_f32_e32 v149, 0x42800000, v126
	v_mul_f32_e32 v0, 0x42800000, v71
	v_cvt_pk_fp8_f32 v133, v139, v149 op_sel:[0,0,1]
	v_mul_f32_e32 v138, 0x42800000, v91
	v_mul_f32_e32 v139, 0x42800000, v111
	v_mul_f32_e32 v149, 0x42800000, v127
	ds_write_b128 v144, v[130:133] offset:32768
	v_mul_f32_e32 v131, 0x42800000, v67
	v_mov_b32_e32 v130, v1
	v_cvt_pk_fp8_f32 v130, v0, v131
	v_mul_f32_e32 v132, 0x42800000, v79
	v_mul_f32_e32 v133, 0x42800000, v75
	v_mul_f32_e32 v0, 0x42800000, v87
	v_cvt_pk_fp8_f32 v130, v132, v133 op_sel:[0,0,1]
	v_mul_f32_e32 v132, 0x42800000, v83
	v_mov_b32_e32 v131, v1
	v_cvt_pk_fp8_f32 v131, v0, v132
	v_mul_f32_e32 v133, 0x42800000, v95
	v_mul_f32_e32 v0, 0x42800000, v99
	v_mov_b32_e32 v132, v1
	v_cvt_pk_fp8_f32 v131, v133, v138 op_sel:[0,0,1]
	v_mul_f32_e32 v133, 0x42800000, v103
	v_cvt_pk_fp8_f32 v132, v0, v133
	v_mul_f32_e32 v138, 0x42800000, v107
	v_mul_f32_e32 v0, 0x42800000, v115
	v_mov_b32_e32 v133, v1
	v_cvt_pk_fp8_f32 v132, v138, v139 op_sel:[0,0,1]
	v_mul_f32_e32 v138, 0x42800000, v119
	v_cvt_pk_fp8_f32 v133, v0, v138
	v_mul_f32_e32 v139, 0x42800000, v123
	v_mul_f32_e32 v0, 0x42800000, v72
	v_mul_f32_e32 v138, 0x42800000, v92
	v_cvt_pk_fp8_f32 v133, v139, v149 op_sel:[0,0,1]
	v_mul_f32_e32 v139, 0x42800000, v112
	v_mul_f32_e32 v149, 0x42800000, v128
	s_cmp_lg_u32 s45, 0
	ds_write_b128 v144, v[130:133] offset:32896
	v_mul_f32_e32 v131, 0x42800000, v68
	v_mov_b32_e32 v130, v1
	v_cvt_pk_fp8_f32 v130, v0, v131
	v_mul_f32_e32 v132, 0x42800000, v80
	v_mul_f32_e32 v133, 0x42800000, v76
	v_mul_f32_e32 v0, 0x42800000, v88
	v_cvt_pk_fp8_f32 v130, v132, v133 op_sel:[0,0,1]
	v_mul_f32_e32 v132, 0x42800000, v84
	v_mov_b32_e32 v131, v1
	v_cvt_pk_fp8_f32 v131, v0, v132
	v_mul_f32_e32 v133, 0x42800000, v96
	v_mul_f32_e32 v0, 0x42800000, v100
	v_mov_b32_e32 v132, v1
	v_cvt_pk_fp8_f32 v131, v133, v138 op_sel:[0,0,1]
	v_mul_f32_e32 v133, 0x42800000, v104
	v_cvt_pk_fp8_f32 v132, v0, v133
	v_mul_f32_e32 v138, 0x42800000, v108
	v_mul_f32_e32 v0, 0x42800000, v116
	v_mov_b32_e32 v133, v1
	v_cvt_pk_fp8_f32 v132, v138, v139 op_sel:[0,0,1]
	v_mul_f32_e32 v138, 0x42800000, v120
	v_cvt_pk_fp8_f32 v133, v0, v138
	v_mul_f32_e32 v139, 0x42800000, v124
	v_mul_f32_e32 v0, 0x42800000, v73
	v_mul_f32_e32 v138, 0x42800000, v93
	v_cvt_pk_fp8_f32 v133, v139, v149 op_sel:[0,0,1]
	v_mul_f32_e32 v139, 0x42800000, v113
	v_mul_f32_e32 v149, 0x42800000, v129
	s_cselect_b64 s[34:35], -1, 0
	ds_write_b128 v144, v[130:133] offset:33024
	v_mul_f32_e32 v131, 0x42800000, v69
	v_mov_b32_e32 v130, v1
	v_cvt_pk_fp8_f32 v130, v0, v131
	v_mul_f32_e32 v132, 0x42800000, v81
	v_mul_f32_e32 v133, 0x42800000, v77
	v_mul_f32_e32 v0, 0x42800000, v89
	v_cvt_pk_fp8_f32 v130, v132, v133 op_sel:[0,0,1]
	v_mul_f32_e32 v132, 0x42800000, v85
	v_mov_b32_e32 v131, v1
	v_cvt_pk_fp8_f32 v131, v0, v132
	v_mul_f32_e32 v133, 0x42800000, v97
	v_mul_f32_e32 v0, 0x42800000, v101
	v_mov_b32_e32 v132, v1
	v_cvt_pk_fp8_f32 v131, v133, v138 op_sel:[0,0,1]
	v_mul_f32_e32 v133, 0x42800000, v105
	v_cvt_pk_fp8_f32 v132, v0, v133
	v_mul_f32_e32 v138, 0x42800000, v109
	v_mul_f32_e32 v0, 0x42800000, v117
	v_mov_b32_e32 v133, v1
	v_cvt_pk_fp8_f32 v132, v138, v139 op_sel:[0,0,1]
	v_mul_f32_e32 v138, 0x42800000, v121
	v_cvt_pk_fp8_f32 v133, v0, v138
	v_mul_f32_e32 v139, 0x42800000, v125
	v_add_u32_e32 v138, s24, v140
	s_cmp_eq_u32 s45, 0
	v_cvt_pk_fp8_f32 v133, v139, v149 op_sel:[0,0,1]
	ds_write_b128 v144, v[130:133] offset:33152
	s_waitcnt lgkmcnt(0)
	s_barrier
	ds_read_b128 v[130:133], v145 offset:32768
	s_cbranch_scc1 .LBB0_1035
	v_cmp_lt_i32_e32 vcc, s47, v138
	v_lshlrev_b32_e32 v0, 1, v138
	v_and_b32_e32 v139, 0x7f, v138
	s_and_saveexec_b64 s[8:9], vcc
	s_xor_b64 s[8:9], exec, s[8:9]
	v_add_u32_e32 v0, 0x7ffff800, v0
	v_and_b32_e32 v0, 0x7fffff00, v0
	v_or3_b32 v138, v139, v0, s64
	s_andn2_saveexec_b64 s[8:9], s[8:9]
	v_and_or_b32 v138, v0, s65, v139
	s_or_b64 exec, exec, s[8:9]
